# next sub-load issued in two halves: first two loads right after staging part 1, last two after staging part 2; part-2 waits re-derived
# baseline (speedup 1.0000x reference)
.LBB1_6:
	s_lshr_b32 s57, s46, 2
	s_lshl_b32 s5, s46, 3
	s_lshl_b32 s4, s47, 3
	s_lshr_b32 s60, s47, 2
	s_add_i32 s59, s57, s51
	s_and_b64 s[4:5], s[4:5], s[38:39]
	s_add_i32 s58, s60, s45
	s_lshl_b32 s59, s59, 5
	v_or_b32_e32 v71, s5, v1
	s_lshl_b32 s58, s58, 5
	v_or_b32_e32 v72, s4, v68
	v_or_b32_e32 v71, s59, v71
	v_or_b32_e32 v72, s58, v72
	v_subrev_u32_e32 v74, s52, v71
	v_subrev_u32_e32 v73, s50, v72
	v_cmp_gt_i32_e32 vcc, s54, v74
	v_add_u32_e32 v75, 0xc8, v74
	v_add_u32_e32 v76, 0xc8, v73
	v_cndmask_b32_e64 v74, 0, 1, vcc
	v_cmp_gt_i32_e32 vcc, s49, v73
	v_cmp_gt_i32_e64 s[4:5], s53, v75
	s_cmp_lt_u32 s57, s55
	v_cndmask_b32_e64 v73, 0, 1, vcc
	v_cmp_gt_i32_e32 vcc, s48, v76
	s_cselect_b64 s[58:59], -1, 0
	s_cmp_lt_u32 s60, s42
	v_cndmask_b32_e64 v76, 0, 1, vcc
	v_cmp_gt_i32_e32 vcc, s50, v72
	v_cndmask_b32_e64 v72, 0, 1, s[4:5]
	v_cmp_gt_i32_e64 s[4:5], s52, v71
	s_cselect_b64 s[60:61], -1, 0
	s_lshl_b32 s62, 1, s46
	v_cndmask_b32_e64 v71, v74, v72, s[4:5]
	v_cndmask_b32_e32 v72, v73, v76, vcc
	v_and_b32_e32 v71, 1, v71
	v_and_b32_e32 v72, 1, v72
	v_cmp_eq_u32_e32 vcc, 1, v71
	s_lshl_b32 s57, 1, s47
	v_mov_b32_e32 v75, s62
	v_cmp_eq_u32_e64 s[4:5], 1, v72
	s_and_b64 vcc, s[58:59], vcc
	v_mov_b32_e32 v77, s57
	v_cndmask_b32_e32 v71, 0, v75, vcc
	s_and_b64 vcc, s[60:61], s[4:5]
	s_add_i32 s47, s47, 2
	s_add_i32 s46, s46, 2
	s_add_i32 s56, s56, -2
	v_cndmask_b32_e32 v72, 0, v77, vcc
	v_or_b32_e32 v70, v71, v70
	s_cmp_lg_u32 s56, 0
	v_or_b32_e32 v69, v72, v69
	s_cbranch_scc1 .LBB1_6
	v_lshrrev_b32_e32 v1, 1, v212
	v_xor_b32_e32 v72, v1, v68
	v_and_b32_e32 v196, 1, v0
	v_bitop3_b32 v1, v1, v68, 8 bitop3:0x1e
	v_lshlrev_b32_e32 v71, 9, v68
	v_lshlrev_b32_e32 v73, 3, v196
	v_lshlrev_b32_e32 v1, 4, v1
	v_or3_b32 v201, v1, v71, v73
	v_lshrrev_b32_e32 v1, 5, v212
	v_lshlrev_b32_e32 v72, 4, v72
	v_and_b32_e32 v68, 0x100, v0
	v_bitop3_b32 v74, v1, v0, 15 bitop3:0x78
	v_and_b32_e32 v214, 31, v0
	v_lshl_or_b32 v204, v214, 9, v68
	v_lshlrev_b32_e32 v203, 4, v74
	v_or3_b32 v202, v72, v71, v73
	v_or_b32_e32 v205, v69, v70
	s_waitcnt vmcnt(23)
	v_cvt_pk_f16_f32 v68, v62, v63
	v_cvt_pk_f16_f32 v69, v64, v65
	ds_write_b64 v202, v[68:69]
	v_and_b32_e32 v68, 1, v205
	v_cmp_eq_u32_e32 vcc, 0, v68
	s_mov_b32 s39, 0
	s_movk_i32 s45, 0x2000
	v_cndmask_b32_e64 v68, 1.0, 0, vcc
	v_pk_fma_f32 v[62:63], v[68:69], v[62:63], 0 op_sel_hi:[0,1,0]
	v_pk_fma_f32 v[64:65], v[68:69], v[64:65], 0 op_sel_hi:[0,1,0]
	s_waitcnt vmcnt(21)
	v_cvt_pk_f16_f32 v68, v58, v59
	v_cvt_pk_f16_f32 v69, v60, v61
	ds_write_b64 v201, v[68:69] offset:4096
	v_and_b32_e32 v68, 2, v205
	v_cmp_eq_u32_e32 vcc, 0, v68
	s_nop 1
	v_cndmask_b32_e64 v68, 1.0, 0, vcc
	v_pk_fma_f32 v[58:59], v[68:69], v[58:59], v[62:63] op_sel_hi:[0,1,1]
	s_waitcnt vmcnt(19)
	v_cvt_pk_f16_f32 v62, v54, v55
	v_cvt_pk_f16_f32 v63, v56, v57
	ds_write_b64 v202, v[62:63] offset:8192
	v_and_b32_e32 v62, 4, v205
	v_cmp_eq_u32_e32 vcc, 0, v62
	v_pk_fma_f32 v[60:61], v[68:69], v[60:61], v[64:65] op_sel_hi:[0,1,1]
	s_nop 0
	v_cndmask_b32_e64 v62, 1.0, 0, vcc
	v_pk_fma_f32 v[54:55], v[62:63], v[54:55], v[58:59] op_sel_hi:[0,1,1]
	s_waitcnt vmcnt(17)
	v_cvt_pk_f16_f32 v58, v50, v51
	v_cvt_pk_f16_f32 v59, v52, v53
	ds_write_b64 v201, v[58:59] offset:12288
	v_and_b32_e32 v58, 8, v205
	v_cmp_eq_u32_e32 vcc, 0, v58
	v_pk_fma_f32 v[56:57], v[62:63], v[56:57], v[60:61] op_sel_hi:[0,1,1]
	s_nop 0
	v_cndmask_b32_e64 v58, 1.0, 0, vcc
	v_pk_fma_f32 v[50:51], v[58:59], v[50:51], v[54:55] op_sel_hi:[0,1,1]
	v_pk_fma_f32 v[52:53], v[58:59], v[52:53], v[56:57] op_sel_hi:[0,1,1]
	v_cvt_pk_f16_f32 v50, v50, v51
	v_cvt_pk_f16_f32 v51, v52, v53
	v_or_b32_e32 v52, 0x20000, v202
	ds_write_b64 v52, v[50:51]
	v_cvt_pk_f16_f32 v50, v46, v47
	v_cvt_pk_f16_f32 v51, v48, v49
	ds_write_b64 v202, v[50:51] offset:16384
	v_and_b32_e32 v50, 16, v205
	v_cmp_eq_u32_e32 vcc, 0, v50
	s_nop 1
	v_cndmask_b32_e64 v50, 1.0, 0, vcc
	v_pk_fma_f32 v[46:47], v[50:51], v[46:47], 0 op_sel_hi:[0,1,0]
	v_pk_fma_f32 v[48:49], v[50:51], v[48:49], 0 op_sel_hi:[0,1,0]
	v_cvt_pk_f16_f32 v50, v42, v43
	v_cvt_pk_f16_f32 v51, v44, v45
	ds_write_b64 v201, v[50:51] offset:20480
	v_and_b32_e32 v50, 32, v205
	v_cmp_eq_u32_e32 vcc, 0, v50
	s_nop 1
	v_cndmask_b32_e64 v50, 1.0, 0, vcc
	v_pk_fma_f32 v[42:43], v[50:51], v[42:43], v[46:47] op_sel_hi:[0,1,1]
	v_cvt_pk_f16_f32 v46, v38, v39
	v_cvt_pk_f16_f32 v47, v40, v41
	ds_write_b64 v202, v[46:47] offset:24576
	v_and_b32_e32 v46, 64, v205
	v_cmp_eq_u32_e32 vcc, 0, v46
	v_pk_fma_f32 v[44:45], v[50:51], v[44:45], v[48:49] op_sel_hi:[0,1,1]
	s_nop 0
	v_cndmask_b32_e64 v46, 1.0, 0, vcc
	v_pk_fma_f32 v[38:39], v[46:47], v[38:39], v[42:43] op_sel_hi:[0,1,1]
	s_waitcnt vmcnt(16)
	v_cvt_pk_f16_f32 v42, v34, v35
	v_cvt_pk_f16_f32 v43, v36, v37
	ds_write_b64 v201, v[42:43] offset:28672
	v_and_b32_e32 v42, 0x80, v205
	v_cmp_eq_u32_e32 vcc, 0, v42
	v_pk_fma_f32 v[40:41], v[46:47], v[40:41], v[44:45] op_sel_hi:[0,1,1]
	s_nop 0
	v_cndmask_b32_e64 v42, 1.0, 0, vcc
	v_pk_fma_f32 v[34:35], v[42:43], v[34:35], v[38:39] op_sel_hi:[0,1,1]
	v_pk_fma_f32 v[36:37], v[42:43], v[36:37], v[40:41] op_sel_hi:[0,1,1]
	v_cvt_pk_f16_f32 v34, v34, v35
	v_cvt_pk_f16_f32 v35, v36, v37
	v_or_b32_e32 v36, 0x21000, v201
	ds_write_b64 v36, v[34:35]
	s_waitcnt vmcnt(15)
	v_cvt_pk_f16_f32 v34, v30, v31
	v_cvt_pk_f16_f32 v35, v32, v33
	ds_write_b64 v202, v[34:35] offset:32768
	v_and_b32_e32 v34, 0x100, v205
	v_cmp_eq_u32_e32 vcc, 0, v34
	s_waitcnt vmcnt(13)
	v_cvt_pk_f16_f32 v34, v26, v27
	v_cvt_pk_f16_f32 v35, v28, v29
	ds_write_b64 v201, v[34:35] offset:36864
	v_and_b32_e32 v34, 0x200, v205
	v_cndmask_b32_e64 v186, 1.0, 0, vcc
	v_cmp_eq_u32_e32 vcc, 0, v34
	v_mov_b32_e32 v187, v186
	v_pk_fma_f32 v[30:31], v[186:187], v[30:31], 0 op_sel_hi:[0,1,0]
	v_cndmask_b32_e64 v188, 1.0, 0, vcc
	v_mov_b32_e32 v189, v188
	v_pk_fma_f32 v[26:27], v[188:189], v[26:27], v[30:31] op_sel_hi:[0,1,1]
	s_waitcnt vmcnt(11)
	v_cvt_pk_f16_f32 v30, v22, v23
	v_cvt_pk_f16_f32 v31, v24, v25
	ds_write_b64 v202, v[30:31] offset:40960
	v_and_b32_e32 v30, 0x400, v205
	v_cmp_eq_u32_e32 vcc, 0, v30
	v_pk_fma_f32 v[32:33], v[186:187], v[32:33], 0 op_sel_hi:[0,1,0]
	v_pk_fma_f32 v[28:29], v[188:189], v[28:29], v[32:33] op_sel_hi:[0,1,1]
	v_cndmask_b32_e64 v190, 1.0, 0, vcc
	v_mov_b32_e32 v191, v190
	v_pk_fma_f32 v[22:23], v[190:191], v[22:23], v[26:27] op_sel_hi:[0,1,1]
	s_waitcnt vmcnt(9)
	v_cvt_pk_f16_f32 v26, v18, v19
	v_cvt_pk_f16_f32 v27, v20, v21
	ds_write_b64 v201, v[26:27] offset:45056
	v_and_b32_e32 v26, 0x800, v205
	v_cmp_eq_u32_e32 vcc, 0, v26
	v_pk_fma_f32 v[24:25], v[190:191], v[24:25], v[28:29] op_sel_hi:[0,1,1]
	s_nop 0
	v_cndmask_b32_e64 v192, 1.0, 0, vcc
	v_mov_b32_e32 v193, v192
	v_pk_fma_f32 v[18:19], v[192:193], v[18:19], v[22:23] op_sel_hi:[0,1,1]
	v_pk_fma_f32 v[20:21], v[192:193], v[20:21], v[24:25] op_sel_hi:[0,1,1]
	v_cvt_pk_f16_f32 v18, v18, v19
	v_cvt_pk_f16_f32 v19, v20, v21
	v_or_b32_e32 v20, 0x22000, v202
	ds_write_b64 v20, v[18:19]
	v_cvt_pk_f16_f32 v18, v14, v15
	v_cvt_pk_f16_f32 v19, v16, v17
	ds_write_b64 v202, v[18:19] offset:49152
	v_and_b32_e32 v18, 0x1000, v205
	v_cmp_eq_u32_e32 vcc, 0, v18
	v_cvt_pk_f16_f32 v18, v10, v11
	v_cvt_pk_f16_f32 v19, v12, v13
	ds_write_b64 v201, v[18:19] offset:53248
	v_and_b32_e32 v18, 0x2000, v205
	v_cndmask_b32_e64 v178, 1.0, 0, vcc
	v_cmp_eq_u32_e32 vcc, 0, v18
	v_mov_b32_e32 v179, v178
	v_pk_fma_f32 v[14:15], v[178:179], v[14:15], 0 op_sel_hi:[0,1,0]
	v_cndmask_b32_e64 v180, 1.0, 0, vcc
	v_mov_b32_e32 v181, v180
	v_pk_fma_f32 v[10:11], v[180:181], v[10:11], v[14:15] op_sel_hi:[0,1,1]
	v_cvt_pk_f16_f32 v14, v6, v7
	v_cvt_pk_f16_f32 v15, v8, v9
	ds_write_b64 v202, v[14:15] offset:57344
	v_and_b32_e32 v14, 0x4000, v205
	v_cmp_eq_u32_e32 vcc, 0, v14
	v_pk_fma_f32 v[16:17], v[178:179], v[16:17], 0 op_sel_hi:[0,1,0]
	v_pk_fma_f32 v[12:13], v[180:181], v[12:13], v[16:17] op_sel_hi:[0,1,1]
	v_cndmask_b32_e64 v182, 1.0, 0, vcc
	v_mov_b32_e32 v183, v182
	v_pk_fma_f32 v[6:7], v[182:183], v[6:7], v[10:11] op_sel_hi:[0,1,1]
	s_waitcnt vmcnt(8)
	v_cvt_pk_f16_f32 v10, v2, v3
	v_cvt_pk_f16_f32 v11, v4, v5
	ds_write_b64 v201, v[10:11] offset:61440
	v_and_b32_e32 v10, 0x8000, v205
	v_cmp_eq_u32_e32 vcc, 0, v10
	v_pk_fma_f32 v[8:9], v[182:183], v[8:9], v[12:13] op_sel_hi:[0,1,1]
	s_nop 0
	v_cndmask_b32_e64 v184, 1.0, 0, vcc
	v_mov_b32_e32 v185, v184
	v_pk_fma_f32 v[2:3], v[184:185], v[2:3], v[6:7] op_sel_hi:[0,1,1]
	v_pk_fma_f32 v[4:5], v[184:185], v[4:5], v[8:9] op_sel_hi:[0,1,1]
	v_cvt_pk_f16_f32 v2, v2, v3
	v_cvt_pk_f16_f32 v3, v4, v5
	v_or_b32_e32 v4, 0x23000, v201
	ds_write_b64 v4, v[2:3]
	v_mov_b32_e32 v2, 0
	s_add_i32 s46, s42, -1
	v_lshl_add_u64 v[194:195], s[40:41], 0, v[66:67]
	v_or_b32_e32 v206, 0x20000, v204
	s_mov_b32 s41, -3
	s_movk_i32 s40, 0x3000
	s_mov_b32 s4, s20
	s_mov_b32 s5, s21
	s_mov_b32 s20, 0
	v_mov_b32_e32 v3, v2
	v_mov_b32_e32 v4, v2
	v_mov_b32_e32 v5, v2
	v_mov_b32_e32 v6, v2
	v_mov_b32_e32 v7, v2
	v_mov_b32_e32 v8, v2
	v_mov_b32_e32 v9, v2
	v_mov_b32_e32 v10, v2
	v_mov_b32_e32 v11, v2
	v_mov_b32_e32 v12, v2
	v_mov_b32_e32 v13, v2
	v_mov_b32_e32 v14, v2
	v_mov_b32_e32 v15, v2
	v_mov_b32_e32 v16, v2
	v_mov_b32_e32 v17, v2
	v_mov_b32_e32 v34, v2
	v_mov_b32_e32 v35, v2
	v_mov_b32_e32 v36, v2
	v_mov_b32_e32 v37, v2
	v_mov_b32_e32 v38, v2
	v_mov_b32_e32 v39, v2
	v_mov_b32_e32 v40, v2
	v_mov_b32_e32 v41, v2
	v_mov_b32_e32 v42, v2
	v_mov_b32_e32 v43, v2
	v_mov_b32_e32 v44, v2
	v_mov_b32_e32 v45, v2
	v_mov_b32_e32 v46, v2
	v_mov_b32_e32 v47, v2
	v_mov_b32_e32 v48, v2
	v_mov_b32_e32 v49, v2
	v_mov_b32_e32 v50, v2
	v_mov_b32_e32 v51, v2
	v_mov_b32_e32 v52, v2
	v_mov_b32_e32 v53, v2
	v_mov_b32_e32 v54, v2
	v_mov_b32_e32 v55, v2
	v_mov_b32_e32 v56, v2
	v_mov_b32_e32 v57, v2
	v_mov_b32_e32 v58, v2
	v_mov_b32_e32 v59, v2
	v_mov_b32_e32 v60, v2
	v_mov_b32_e32 v61, v2
	v_mov_b32_e32 v62, v2
	v_mov_b32_e32 v63, v2
	v_mov_b32_e32 v64, v2
	v_mov_b32_e32 v65, v2
	v_mov_b32_e32 v18, v2
	v_mov_b32_e32 v19, v2
	v_mov_b32_e32 v20, v2
	v_mov_b32_e32 v21, v2
	v_mov_b32_e32 v22, v2
	v_mov_b32_e32 v23, v2
	v_mov_b32_e32 v24, v2
	v_mov_b32_e32 v25, v2
	v_mov_b32_e32 v26, v2
	v_mov_b32_e32 v27, v2
	v_mov_b32_e32 v28, v2
	v_mov_b32_e32 v29, v2
	v_mov_b32_e32 v30, v2
	v_mov_b32_e32 v31, v2
	v_mov_b32_e32 v32, v2
	v_mov_b32_e32 v33, v2
	v_mov_b32_e32 v66, v2
	v_mov_b32_e32 v67, v2
	v_mov_b32_e32 v68, v2
	v_mov_b32_e32 v69, v2
	v_mov_b32_e32 v70, v2
	v_mov_b32_e32 v71, v2
	v_mov_b32_e32 v72, v2
	v_mov_b32_e32 v73, v2
	v_mov_b32_e32 v74, v2
	v_mov_b32_e32 v75, v2
	v_mov_b32_e32 v76, v2
	v_mov_b32_e32 v77, v2
	v_mov_b32_e32 v78, v2
	v_mov_b32_e32 v79, v2
	v_mov_b32_e32 v80, v2
	v_mov_b32_e32 v81, v2
	s_add_i32 s75, s44, 1
	s_lshl_b32 s75, s75, 10
	s_and_b32 s75, s75, 0x1c00
	s_min_u32 s76, 2, s46
	s_lshl_b32 s76, s76, 18
	s_or_b32 s75, s75, s76
	s_mov_b32 s76, 0
	v_add_u32_e32 v174, s76, v197
	v_add_u32_e32 v170, s76, v198
	v_add_u32_e32 v162, s76, v199
	v_add_u32_e32 v154, s76, v200
	buffer_load_dwordx4 v[174:177], v174, s[4:7], s75 offen sc0 nt sc1
	buffer_load_dwordx4 v[170:173], v170, s[4:7], s75 offen sc0 nt sc1
	buffer_load_dwordx4 v[162:165], v162, s[4:7], s75 offen sc0 nt sc1
	buffer_load_dwordx4 v[154:157], v154, s[4:7], s75 offen sc0 nt sc1
	s_waitcnt lgkmcnt(0)
	s_barrier

.Lsteady_w1:
	s_waitcnt vmcnt(19)
	v_cvt_pk_f16_f32 v234, v142, v143
	v_cvt_pk_f16_f32 v235, v144, v145
	v_or_b32_e32 v236, s38, v202
	ds_write_b64 v236, v[234:235]
	v_bfe_u32 v234, v205, s53, 1
	v_cmp_eq_u32_e32 vcc, 0, v234
	v_lshrrev_b32_e32 v241, s53, v205
	s_waitcnt vmcnt(18)
	v_cvt_pk_f16_f32 v236, v138, v139
	v_cndmask_b32_e64 v234, 1.0, 0, vcc
	v_pk_fma_f32 v[142:143], v[234:235], v[142:143], 0 op_sel_hi:[0,1,0]
	v_cvt_pk_f16_f32 v237, v140, v141
	v_or_b32_e32 v235, s38, v201
	ds_write_b64 v235, v[236:237] offset:4096
	v_and_b32_e32 v235, 2, v241
	v_cmp_eq_u32_e32 vcc, 0, v235
	s_add_i32 s52, s41, 7
	s_nop 0
	v_cndmask_b32_e64 v236, 1.0, 0, vcc
	v_pk_fma_f32 v[238:239], v[236:237], v[138:139], v[142:143] op_sel_hi:[0,1,1]
	v_xor_b32_e32 v215, 32, v215
	s_waitcnt lgkmcnt(6)
	v_mfma_f32_32x32x16_f16 v[2:17], v[118:121], v[208:211], v[2:17]
	v_add_u32_e32 v207, v207, v215
	v_fma_f32 v138, v234, v144, 0
	v_fma_f32 v139, v234, v145, 0
	s_waitcnt lgkmcnt(5)
	v_mfma_f32_32x32x16_f16 v[34:49], v[118:121], v[216:219], v[34:49]
	s_waitcnt lgkmcnt(4)
	v_mfma_f32_32x32x16_f16 v[50:65], v[118:121], v[220:223], v[50:65]
	v_fma_f32 v220, v236, v140, v138
	v_fma_f32 v221, v236, v141, v139
	s_add_i32 s75, s21, 7
	s_and_b32 s76, s75, 3
	s_lshr_b32 s75, s75, 2
	s_add_i32 s75, s75, s44
	s_min_u32 s76, s76, s46
	s_lshl_b32 s75, s75, 10
	s_and_b32 s75, s75, 0x1c00
	s_lshl_b32 s76, s76, 18
	s_or_b32 s75, s75, s76
	s_cmp_lt_u32 s21, 25
	s_cselect_b32 s76, 0, 2.0
	v_add_u32_e32 v142, s76, v197
	v_add_u32_e32 v138, s76, v198
	buffer_load_dwordx4 v[142:145], v142, s[4:7], s75 offen sc0 nt sc1
	buffer_load_dwordx4 v[138:141], v138, s[4:7], s75 offen sc0 nt sc1
	v_add_u32_e32 v254, v240, v215
	s_waitcnt lgkmcnt(3)
	v_mfma_f32_32x32x16_f16 v[18:33], v[118:121], v[226:229], v[18:33]
	ds_read_b128 v[118:121], v207
	ds_read_b128 v[250:253], v207 offset:16384
	ds_read_b128 v[208:211], v207 offset:32768
	ds_read_b128 v[216:219], v207 offset:49152
	ds_read_b128 v[234:237], v254
	s_waitcnt lgkmcnt(7)
	v_mfma_f32_32x32x16_f16 v[66:81], v[114:117], v[230:233], v[66:81]
	s_bfe_u32 s38, s52, 0x10002
	s_lshl_b32 s53, s38, 16
	s_or_b32 s49, s53, s49
	s_waitcnt vmcnt(19)
	v_cvt_pk_f16_f32 v114, v134, v135
	v_cvt_pk_f16_f32 v115, v136, v137
	v_or_b32_e32 v116, s49, v202
	ds_write_b64 v116, v[114:115] offset:8192
	v_and_b32_e32 v114, 4, v241
	v_cmp_eq_u32_e32 vcc, 0, v114
	s_lshl_b32 s38, s38, 14
	s_nop 0
	v_cndmask_b32_e64 v114, 1.0, 0, vcc
	v_pk_fma_f32 v[116:117], v[114:115], v[134:135], v[238:239] op_sel_hi:[0,1,1]
	v_pk_fma_f32 v[114:115], v[114:115], v[136:137], v[220:221] op_sel_hi:[0,1,1]
	s_waitcnt vmcnt(18)
	v_cvt_pk_f16_f32 v134, v130, v131
	v_cvt_pk_f16_f32 v135, v132, v133
	v_or_b32_e32 v136, s49, v201
	s_lshl_b32 s49, s51, 12
	ds_write_b64 v136, v[134:135] offset:12288
	v_and_b32_e32 v134, 8, v241
	s_or_b32 s38, s38, s49
	v_cmp_eq_u32_e32 vcc, 0, v134
	s_bitcmp0_b32 s21, 0
	s_nop 0
	v_cndmask_b32_e64 v134, 1.0, 0, vcc
	s_cselect_b64 vcc, -1, 0
	v_pk_fma_f32 v[116:117], v[134:135], v[130:131], v[116:117] op_sel_hi:[0,1,1]
	v_pk_fma_f32 v[114:115], v[134:135], v[132:133], v[114:115] op_sel_hi:[0,1,1]
	v_cndmask_b32_e32 v207, v201, v202, vcc
	v_cvt_pk_f16_f32 v116, v116, v117
	v_cvt_pk_f16_f32 v117, v114, v115
	v_or_b32_e32 v114, s38, v207
	v_or_b32_e32 v114, 0x20000, v114
	ds_write_b64 v114, v[116:117]
	v_add_u32_e32 v134, s76, v199
	v_add_u32_e32 v130, s76, v200
	buffer_load_dwordx4 v[134:137], v134, s[4:7], s75 offen sc0 nt sc1
	buffer_load_dwordx4 v[130:133], v130, s[4:7], s75 offen sc0 nt sc1
	s_waitcnt lgkmcnt(7)
	v_mfma_f32_32x32x16_f16 v[2:17], v[90:93], v[118:121], v[2:17]
	s_waitcnt lgkmcnt(6)
	v_mfma_f32_32x32x16_f16 v[34:49], v[90:93], v[250:253], v[34:49]
	s_waitcnt lgkmcnt(5)
	v_mfma_f32_32x32x16_f16 v[50:65], v[90:93], v[208:211], v[50:65]
	s_waitcnt lgkmcnt(4)
	v_mfma_f32_32x32x16_f16 v[18:33], v[90:93], v[216:219], v[18:33]
	s_waitcnt lgkmcnt(3)
	v_mfma_f32_32x32x16_f16 v[66:81], v[98:101], v[234:237], v[66:81]
	s_cmp_lg_u32 s51, 3
	s_cbranch_scc1 .LBB1_10
	s_waitcnt lgkmcnt(0)
	s_barrier
.LBB1_10:
	s_add_i32 s38, s41, 6
	s_lshr_b32 s38, s38, 2
	s_add_i32 s38, s38, s44
	s_lshl_b32 s38, s38, 17
	s_add_i32 s49, s20, 0xc000
	s_and_b32 s38, s38, 0xe0000
	s_and_b32 s53, s49, 0xc000
	s_or_b32 s38, s38, s53
	v_lshl_add_u64 v[90:91], v[194:195], 0, s[38:39]
	s_add_i32 s38, s41, 10
	s_and_b32 s53, s38, 3
	s_lshr_b32 s38, s38, 2
	s_add_i32 s38, s38, s44
	v_add_co_u32_e32 v92, vcc, 0x1000, v90
	s_min_u32 s53, s53, s46
	s_lshl_b32 s38, s38, 10
	v_addc_co_u32_e32 v93, vcc, 0, v91, vcc
	s_and_b32 s38, s38, 0x1c00
	s_lshl_b32 s53, s53, 18
	global_load_dwordx4 v[118:121], v[90:91], off
	global_load_dwordx4 v[114:117], v[92:93], off
	v_add_co_u32_e32 v92, vcc, 0x2000, v90
	s_or_b32 s38, s38, s53
	s_nop 0
	v_addc_co_u32_e32 v93, vcc, 0, v91, vcc
	s_cmp_lt_u32 s21, 25
	v_add_co_u32_e32 v98, vcc, 0x3000, v90
	s_cselect_b32 s53, 0, 2.0
	s_nop 0
	v_addc_co_u32_e32 v99, vcc, 0, v91, vcc
	global_load_dwordx4 v[90:93], v[92:93], off
	s_nop 0
	global_load_dwordx4 v[98:101], v[98:99], off
	s_nop 0
	s_nop 0
	s_add_i32 s38, s41, 4
	s_bfe_u32 s53, s38, 0x10002
	s_and_b32 s38, s38, 3
	s_lshl_b32 s54, s38, 6
	v_lshl_or_b32 v215, s53, 16, v204
	v_xor_b32_e32 v240, s54, v203
	v_add_u32_e32 v226, v215, v240
	ds_read_b128 v[208:211], v226
	ds_read_b128 v[216:219], v226 offset:16384
	ds_read_b128 v[220:223], v226 offset:32768
	ds_read_b128 v[226:229], v226 offset:49152
	v_lshl_add_u32 v241, s53, 14, v206
	v_add_u32_e32 v230, v241, v240
	ds_read_b128 v[230:233], v230
	s_add_i32 s53, s41, 8
	s_and_b32 s54, s53, 3
	s_add_i32 s55, s20, 0x14000
	s_and_b32 s55, s55, 0x10000
	s_lshl_b32 s56, s54, 14
	s_or_b32 s55, s55, s56
	s_lshl_b32 s57, s54, 2
	s_waitcnt vmcnt(19)
	v_cvt_pk_f16_f32 v234, v126, v127
	v_cvt_pk_f16_f32 v235, v128, v129
	v_or_b32_e32 v236, s55, v202
	ds_write_b64 v236, v[234:235]
	v_bfe_u32 v234, v205, s57, 1
	v_cmp_eq_u32_e32 vcc, 0, v234
	v_lshrrev_b32_e32 v242, s57, v205
	s_waitcnt vmcnt(18)
	v_cvt_pk_f16_f32 v236, v122, v123
	v_cndmask_b32_e64 v234, 1.0, 0, vcc
	v_pk_fma_f32 v[126:127], v[234:235], v[126:127], 0 op_sel_hi:[0,1,0]
	v_cvt_pk_f16_f32 v237, v124, v125
	v_or_b32_e32 v235, s55, v201
	ds_write_b64 v235, v[236:237] offset:4096
	v_and_b32_e32 v235, 2, v242
	v_cmp_eq_u32_e32 vcc, 0, v235
	s_nop 1
	v_cndmask_b32_e64 v236, 1.0, 0, vcc
	v_pk_fma_f32 v[238:239], v[236:237], v[122:123], v[126:127] op_sel_hi:[0,1,1]
	s_waitcnt lgkmcnt(4)
	v_mfma_f32_32x32x16_f16 v[50:65], v[102:105], v[220:223], v[50:65]
	v_xor_b32_e32 v222, 32, v240
	v_add_u32_e32 v215, v215, v222
	v_fma_f32 v122, v234, v128, 0
	v_fma_f32 v123, v234, v129, 0
	v_fma_f32 v220, v236, v124, v122
	v_fma_f32 v221, v236, v125, v123
	s_add_i32 s75, s21, 8
	s_and_b32 s76, s75, 3
	s_lshr_b32 s75, s75, 2
	s_add_i32 s75, s75, s44
	s_min_u32 s76, s76, s46
	s_lshl_b32 s75, s75, 10
	s_and_b32 s75, s75, 0x1c00
	s_lshl_b32 s76, s76, 18
	s_or_b32 s75, s75, s76
	s_cmp_lt_u32 s21, 24
	s_cselect_b32 s76, 0, 2.0
	v_add_u32_e32 v126, s76, v197
	v_add_u32_e32 v122, s76, v198
	buffer_load_dwordx4 v[126:129], v126, s[4:7], s75 offen sc0 nt sc1
	buffer_load_dwordx4 v[122:125], v122, s[4:7], s75 offen sc0 nt sc1
	v_add_u32_e32 v254, v241, v222
	v_mfma_f32_32x32x16_f16 v[2:17], v[102:105], v[208:211], v[2:17]
	v_mfma_f32_32x32x16_f16 v[34:49], v[102:105], v[216:219], v[34:49]
	s_waitcnt lgkmcnt(3)
	v_mfma_f32_32x32x16_f16 v[18:33], v[102:105], v[226:229], v[18:33]
	ds_read_b128 v[102:105], v215
	ds_read_b128 v[250:253], v215 offset:16384
	ds_read_b128 v[208:211], v215 offset:32768
	ds_read_b128 v[216:219], v215 offset:49152
	ds_read_b128 v[234:237], v254
	s_waitcnt lgkmcnt(7)
	v_mfma_f32_32x32x16_f16 v[66:81], v[94:97], v[230:233], v[66:81]
	s_bfe_u32 s55, s53, 0x10002
	s_lshl_b32 s57, s55, 16
	s_or_b32 s56, s57, s56
	s_waitcnt vmcnt(19)
	v_cvt_pk_f16_f32 v94, v110, v111
	v_cvt_pk_f16_f32 v95, v112, v113
	v_or_b32_e32 v96, s56, v202
	ds_write_b64 v96, v[94:95] offset:8192
	v_and_b32_e32 v94, 4, v242
	v_cmp_eq_u32_e32 vcc, 0, v94
	s_lshl_b32 s55, s55, 14
	s_lshl_b32 s54, s54, 12
	v_cndmask_b32_e64 v94, 1.0, 0, vcc
	v_pk_fma_f32 v[96:97], v[94:95], v[110:111], v[238:239] op_sel_hi:[0,1,1]
	v_pk_fma_f32 v[94:95], v[94:95], v[112:113], v[220:221] op_sel_hi:[0,1,1]
	s_waitcnt vmcnt(18)
	v_cvt_pk_f16_f32 v110, v106, v107
	v_cvt_pk_f16_f32 v111, v108, v109
	v_or_b32_e32 v112, s56, v201
	ds_write_b64 v112, v[110:111] offset:12288
	v_and_b32_e32 v110, 8, v242
	v_cmp_eq_u32_e32 vcc, 0, v110
	s_or_b32 s54, s55, s54
	s_bitcmp0_b32 s53, 0
	v_cndmask_b32_e64 v110, 1.0, 0, vcc
	v_pk_fma_f32 v[96:97], v[110:111], v[106:107], v[96:97] op_sel_hi:[0,1,1]
	v_pk_fma_f32 v[94:95], v[110:111], v[108:109], v[94:95] op_sel_hi:[0,1,1]
	s_cselect_b64 vcc, -1, 0
	v_cvt_pk_f16_f32 v96, v96, v97
	v_cvt_pk_f16_f32 v97, v94, v95
	v_cndmask_b32_e32 v94, v201, v202, vcc
	v_or_b32_e32 v94, s54, v94
	v_or_b32_e32 v94, 0x20000, v94
	ds_write_b64 v94, v[96:97]
	v_add_u32_e32 v110, s76, v199
	v_add_u32_e32 v106, s76, v200
	buffer_load_dwordx4 v[110:113], v110, s[4:7], s75 offen sc0 nt sc1
	buffer_load_dwordx4 v[106:109], v106, s[4:7], s75 offen sc0 nt sc1
	s_waitcnt lgkmcnt(7)
	v_mfma_f32_32x32x16_f16 v[2:17], v[82:85], v[102:105], v[2:17]
	s_waitcnt lgkmcnt(6)
	v_mfma_f32_32x32x16_f16 v[34:49], v[82:85], v[250:253], v[34:49]
	s_waitcnt lgkmcnt(5)
	v_mfma_f32_32x32x16_f16 v[50:65], v[82:85], v[208:211], v[50:65]
	s_waitcnt lgkmcnt(4)
	v_mfma_f32_32x32x16_f16 v[18:33], v[82:85], v[216:219], v[18:33]
	s_waitcnt lgkmcnt(3)
	v_mfma_f32_32x32x16_f16 v[66:81], v[86:89], v[234:237], v[66:81]
	s_cmp_lg_u32 s38, 3
	s_cbranch_scc1 .LBB1_12
	s_waitcnt lgkmcnt(0)
	s_barrier
.LBB1_12:
	s_lshr_b32 s38, s52, 2
	s_add_i32 s38, s38, s44
	s_lshl_b32 s38, s38, 17
	s_and_b32 s38, s38, 0xe0000
	s_and_b32 s52, s20, 0xc000
	s_or_b32 s38, s38, s52
	v_lshl_add_u64 v[82:83], v[194:195], 0, s[38:39]
	s_add_i32 s38, s41, 11
	s_lshr_b32 s38, s38, 2
	s_add_i32 s38, s38, s44
	v_add_co_u32_e32 v84, vcc, 0x1000, v82
	s_min_u32 s41, s51, s46
	s_lshl_b32 s38, s38, 10
	v_addc_co_u32_e32 v85, vcc, 0, v83, vcc
	s_and_b32 s38, s38, 0x1c00
	s_lshl_b32 s41, s41, 18
	global_load_dwordx4 v[102:105], v[82:83], off
	global_load_dwordx4 v[94:97], v[84:85], off
	v_add_co_u32_e32 v84, vcc, 0x2000, v82
	s_or_b32 s38, s38, s41
	s_nop 0
	v_addc_co_u32_e32 v85, vcc, 0, v83, vcc
	s_cmp_lt_u32 s21, 24
	v_add_co_u32_e32 v86, vcc, 0x3000, v82
	s_cselect_b32 s41, 0, 2.0
	s_nop 0
	v_addc_co_u32_e32 v87, vcc, 0, v83, vcc
	global_load_dwordx4 v[82:85], v[84:85], off
	s_nop 0
	global_load_dwordx4 v[86:89], v[86:87], off
	s_nop 0
	s_nop 0
	s_and_b32 s41, s50, 3
	s_bfe_u32 s38, s50, 0x10002
	s_lshl_b32 s50, s41, 6
	v_lshl_or_b32 v215, s38, 16, v204
	v_xor_b32_e32 v240, s50, v203
	v_add_u32_e32 v226, v215, v240
	ds_read_b128 v[208:211], v226
	ds_read_b128 v[216:219], v226 offset:16384
	ds_read_b128 v[220:223], v226 offset:32768
	ds_read_b128 v[226:229], v226 offset:49152
	v_lshl_add_u32 v241, s38, 14, v206
	v_add_u32_e32 v230, v241, v240
	ds_read_b128 v[230:233], v230
	s_add_i32 s20, s20, 0x18000
	s_and_b32 s20, s20, 0x10000
	s_lshl_b32 s38, s47, 14
	s_or_b32 s20, s20, s38
	s_lshl_b32 s50, s47, 2
	s_waitcnt vmcnt(19)
	v_cvt_pk_f16_f32 v234, v174, v175
	v_cvt_pk_f16_f32 v235, v176, v177
	v_or_b32_e32 v236, s20, v202
	ds_write_b64 v236, v[234:235]
	v_bfe_u32 v234, v205, s50, 1
	v_cmp_eq_u32_e32 vcc, 0, v234
	v_lshrrev_b32_e32 v242, s50, v205
	s_waitcnt vmcnt(17)
	v_cvt_pk_f16_f32 v236, v170, v171
	v_cndmask_b32_e64 v234, 1.0, 0, vcc
	v_pk_fma_f32 v[174:175], v[234:235], v[174:175], 0 op_sel_hi:[0,1,0]
	v_cvt_pk_f16_f32 v237, v172, v173
	v_or_b32_e32 v235, s20, v201
	ds_write_b64 v235, v[236:237] offset:4096
	v_and_b32_e32 v235, 2, v242
	v_cmp_eq_u32_e32 vcc, 0, v235
	s_nop 1
	v_cndmask_b32_e64 v236, 1.0, 0, vcc
	v_pk_fma_f32 v[238:239], v[236:237], v[170:171], v[174:175] op_sel_hi:[0,1,1]
	s_waitcnt lgkmcnt(4)
	v_mfma_f32_32x32x16_f16 v[50:65], v[166:169], v[220:223], v[50:65]
	v_xor_b32_e32 v222, 32, v240
	v_add_u32_e32 v215, v215, v222
	v_fma_f32 v170, v234, v176, 0
	v_fma_f32 v171, v234, v177, 0
	v_fma_f32 v220, v236, v172, v170
	v_fma_f32 v221, v236, v173, v171
	s_cmp_gt_u32 s21, 26
	s_cbranch_scc1 .Lskip_ca
	s_add_i32 s75, s21, 9
	s_and_b32 s76, s75, 3
	s_lshr_b32 s75, s75, 2
	s_add_i32 s75, s75, s44
	s_min_u32 s76, s76, s46
	s_lshl_b32 s75, s75, 10
	s_and_b32 s75, s75, 0x1c00
	s_lshl_b32 s76, s76, 18
	s_or_b32 s75, s75, s76
	s_cmp_lt_u32 s21, 23
	s_cselect_b32 s76, 0, 2.0
	v_add_u32_e32 v174, s76, v197
	v_add_u32_e32 v170, s76, v198
	buffer_load_dwordx4 v[174:177], v174, s[4:7], s75 offen sc0 nt sc1
	buffer_load_dwordx4 v[170:173], v170, s[4:7], s75 offen sc0 nt sc1
.Lskip_ca:
	v_add_u32_e32 v254, v241, v222
	v_mfma_f32_32x32x16_f16 v[2:17], v[166:169], v[208:211], v[2:17]
	v_mfma_f32_32x32x16_f16 v[34:49], v[166:169], v[216:219], v[34:49]
	s_waitcnt lgkmcnt(3)
	v_mfma_f32_32x32x16_f16 v[18:33], v[166:169], v[226:229], v[18:33]
	ds_read_b128 v[166:169], v215
	ds_read_b128 v[250:253], v215 offset:16384
	ds_read_b128 v[208:211], v215 offset:32768
	ds_read_b128 v[216:219], v215 offset:49152
	ds_read_b128 v[234:237], v254
	s_waitcnt lgkmcnt(7)
	v_mfma_f32_32x32x16_f16 v[66:81], v[158:161], v[230:233], v[66:81]
	s_bfe_u32 s20, s48, 0x10002
	s_lshl_b32 s48, s20, 16
	s_or_b32 s38, s48, s38
	s_waitcnt vmcnt(19)
	v_cvt_pk_f16_f32 v158, v162, v163
	v_cvt_pk_f16_f32 v159, v164, v165
	v_or_b32_e32 v160, s38, v202
	ds_write_b64 v160, v[158:159] offset:8192
	v_and_b32_e32 v158, 4, v242
	v_cmp_eq_u32_e32 vcc, 0, v158
	s_lshl_b32 s20, s20, 14
	s_nop 0
	v_cndmask_b32_e64 v158, 1.0, 0, vcc
	v_pk_fma_f32 v[160:161], v[158:159], v[162:163], v[238:239] op_sel_hi:[0,1,1]
	v_pk_fma_f32 v[158:159], v[158:159], v[164:165], v[220:221] op_sel_hi:[0,1,1]
	s_waitcnt vmcnt(18)
	v_cvt_pk_f16_f32 v162, v154, v155
	v_cvt_pk_f16_f32 v163, v156, v157
	v_or_b32_e32 v164, s38, v201
	ds_write_b64 v164, v[162:163] offset:12288
	v_and_b32_e32 v162, 8, v242
	v_cmp_eq_u32_e32 vcc, 0, v162
	s_lshl_b32 s38, s47, 12
	s_or_b32 s20, s20, s38
	v_cndmask_b32_e64 v162, 1.0, 0, vcc
	v_pk_fma_f32 v[154:155], v[162:163], v[154:155], v[160:161] op_sel_hi:[0,1,1]
	v_pk_fma_f32 v[156:157], v[162:163], v[156:157], v[158:159] op_sel_hi:[0,1,1]
	v_cvt_pk_f16_f32 v154, v154, v155
	v_cvt_pk_f16_f32 v155, v156, v157
	v_or_b32_e32 v156, s20, v207
	v_or_b32_e32 v156, 0x20000, v156
	ds_write_b64 v156, v[154:155]
	s_cmp_gt_u32 s21, 26
	s_cbranch_scc0 .Lissue_cb
	s_waitcnt vmcnt(16)
	s_branch .Ldone_cb
.Lissue_cb:
	v_add_u32_e32 v162, s76, v199
	v_add_u32_e32 v154, s76, v200
	buffer_load_dwordx4 v[162:165], v162, s[4:7], s75 offen sc0 nt sc1
	buffer_load_dwordx4 v[154:157], v154, s[4:7], s75 offen sc0 nt sc1
